# baseline (speedup 1.0000x reference)
_Z6k_gemmPKfS0_PK15HIP_vector_typeIjLj4EEPDF16_PKh:
	s_load_dwordx4 s[20:23], s[0:1], 0x0
	s_load_dwordx4 s[4:7], s[0:1], 0x10
	s_load_dwordx2 s[38:39], s[0:1], 0x20
	v_readfirstlane_b32 s8, v0
	v_and_b32_e32 v1, 63, v0
	s_nop 3
	s_lshr_b32 s8, s8, 6
	s_and_b32 s40, s2, 7
	s_lshr_b32 s41, s2, 3
	s_mul_i32 s18, s40, 0x187
	s_min_u32 s19, s18, 0xaae
	s_add_i32 s18, s18, s41
	s_sub_i32 s33, s19, s18
	s_addk_i32 s33, 0x1c6
	s_ashr_i32 s9, s33, 6
	s_max_i32 s9, s9, 0
	s_cmp_eq_u32 s9, 0
	s_cbranch_scc1 .Lg_end
	s_add_i32 s11, s9, 4
	s_lshl_b32 s18, s18, 4
	s_lshl_b32 s19, s8, 2
	s_add_i32 s33, s18, s19
	s_mul_i32 s12, s33, 0x4b0
	s_lshl_b32 s32, s18, 8
	s_sub_u32 s32, s32, 0x100000
	s_mov_b32 s10, 0
	v_lshl_add_u32 v253, v1, 10, s33
	v_mov_b32_e32 v247, 0
	v_cmp_gt_i32_e32 vcc, s9, v1
	s_mov_b32 s18, 0xc350
	v_cmp_gt_i32_e64 s[36:37], s18, v253
	s_and_b64 vcc, vcc, s[36:37]
	s_waitcnt lgkmcnt(0)
	s_and_saveexec_b64 s[36:37], vcc
	global_load_dword v247, v253, s[38:39]
	s_mov_b64 exec, s[36:37]
	s_mov_b32 s24, s22
	s_and_b32 s25, s23, 0xffff
	s_mov_b32 s26, 0x3938700
	s_mov_b32 s27, 0x20000
	s_and_b32 s21, s21, 0xffff
	s_mov_b32 s22, 0x3938700
	s_mov_b32 s23, 0x20000
	s_mov_b32 s28, s6
	s_and_b32 s29, s7, 0xffff
	s_mov_b32 s30, 0xc35000
	s_mov_b32 s31, 0x20000
	v_lshlrev_b32_e32 v238, 4, v1
	v_mul_u32_u24_e32 v253, 0x1746, v1
	v_lshrrev_b32_e32 v253, 16, v253
	v_min_u32_e32 v253, 3, v253
	v_mul_u32_u24_e32 v254, 11, v253
	v_sub_u32_e32 v254, v1, v254
	v_lshlrev_b32_e32 v240, 3, v253
	v_mul_u32_u24_e32 v249, 0x4b0, v253
	v_lshl_add_u32 v249, v254, 4, v249
	v_add_u32_e32 v249, 0x400, v249
	v_mov_b32_e32 v255, 0x80000000
	v_cmp_gt_u32_e64 s[34:35], 44, v1
	s_nop 1
	v_cndmask_b32_e64 v239, v255, v249, s[34:35]
	v_lshl_add_u32 v250, s8, 2, v253
	v_mul_u32_u24_e32 v250, 0x4e0, v250
	v_lshl_add_u32 v250, v254, 3, v250
	v_add_u32_e32 v242, 0x200, v250
	s_mul_i32 s18, s8, 0x1380
	v_lshl_add_u32 v241, v1, 3, s18
	v_and_b32_e32 v249, 15, v1
	v_lshrrev_b32_e32 v250, 4, v1
	v_mul_u32_u24_e32 v243, 0x4e0, v249
	v_lshl_add_u32 v243, v250, 4, v243
	v_mul_u32_u24_e32 v244, 0x440, v250
	v_lshl_add_u32 v244, v249, 1, v244
	s_lshl_b32 s18, s8, 6
	s_add_i32 s18, s18, 39936
	v_add_u32_e32 v244, s18, v244
	v_lshrrev_b32_e32 v249, 4, v0
	v_and_b32_e32 v250, 15, v0
	v_mul_u32_u24_e32 v245, 0x110, v249
	v_lshl_add_u32 v245, v250, 4, v245
	v_add_u32_e32 v245, 39936, v245
	v_lshlrev_b32_e32 v246, 8, v249
	v_lshl_add_u32 v246, v250, 4, v246
	s_lshl_b32 s18, s8, 12
	s_add_i32 s18, s18, 48640
	v_lshl_add_u32 v248, v1, 4, s18
	v_cmp_gt_u32_e32 vcc, 32, v0
	s_and_saveexec_b64 s[36:37], vcc
	v_mul_u32_u24_e32 v251, 0x4e00, v249
	v_mul_u32_u24_e32 v252, 0x4e0, v250
	v_add_u32_e32 v254, v251, v252
	v_mov_b32_e32 v250, 0
	v_mov_b32_e32 v251, 0
	v_mov_b32_e32 v252, 0
	v_mov_b32_e32 v253, 0
	ds_write_b128 v254, v[250:253] offset:1200
	s_mov_b64 exec, s[36:37]
	s_lshl_b32 s18, s8, 11
	v_lshl_add_u32 v253, v1, 4, s18
	v_add_u32_e32 v254, 0x22000, v253
	global_load_dwordx4 v[138:141], v254, s[4:5]
	global_load_dwordx4 v[142:145], v254, s[4:5] offset:1024
	v_add_u32_e32 v254, 0x2000, v254
	global_load_dwordx4 v[146:149], v254, s[4:5]
	global_load_dwordx4 v[150:153], v254, s[4:5] offset:1024
	global_load_dwordx4 v[2:5], v253, s[4:5]
	global_load_dwordx4 v[6:9], v253, s[4:5] offset:1024
	v_add_u32_e32 v253, 0x2000, v253
	global_load_dwordx4 v[10:13], v253, s[4:5]
	global_load_dwordx4 v[14:17], v253, s[4:5] offset:1024
	v_add_u32_e32 v253, 0x2000, v253
	global_load_dwordx4 v[18:21], v253, s[4:5]
	global_load_dwordx4 v[22:25], v253, s[4:5] offset:1024
	v_add_u32_e32 v253, 0x2000, v253
	global_load_dwordx4 v[26:29], v253, s[4:5]
	global_load_dwordx4 v[30:33], v253, s[4:5] offset:1024
	v_add_u32_e32 v253, 0x2000, v253
	global_load_dwordx4 v[34:37], v253, s[4:5]
	global_load_dwordx4 v[38:41], v253, s[4:5] offset:1024
	v_add_u32_e32 v253, 0x2000, v253
	global_load_dwordx4 v[42:45], v253, s[4:5]
	global_load_dwordx4 v[46:49], v253, s[4:5] offset:1024
	v_add_u32_e32 v253, 0x2000, v253
	global_load_dwordx4 v[50:53], v253, s[4:5]
	global_load_dwordx4 v[54:57], v253, s[4:5] offset:1024
	v_add_u32_e32 v253, 0x2000, v253
	global_load_dwordx4 v[58:61], v253, s[4:5]
	global_load_dwordx4 v[62:65], v253, s[4:5] offset:1024
	v_add_u32_e32 v253, 0x2000, v253
	global_load_dwordx4 v[66:69], v253, s[4:5]
	global_load_dwordx4 v[70:73], v253, s[4:5] offset:1024
	v_add_u32_e32 v253, 0x2000, v253
	global_load_dwordx4 v[74:77], v253, s[4:5]
	global_load_dwordx4 v[78:81], v253, s[4:5] offset:1024
	v_add_u32_e32 v253, 0x2000, v253
	global_load_dwordx4 v[82:85], v253, s[4:5]
	global_load_dwordx4 v[86:89], v253, s[4:5] offset:1024
	v_add_u32_e32 v253, 0x2000, v253
	global_load_dwordx4 v[90:93], v253, s[4:5]
	global_load_dwordx4 v[94:97], v253, s[4:5] offset:1024
	v_add_u32_e32 v253, 0x2000, v253
	global_load_dwordx4 v[98:101], v253, s[4:5]
	global_load_dwordx4 v[102:105], v253, s[4:5] offset:1024
	v_add_u32_e32 v253, 0x2000, v253
	global_load_dwordx4 v[106:109], v253, s[4:5]
	global_load_dwordx4 v[110:113], v253, s[4:5] offset:1024
	v_add_u32_e32 v253, 0x2000, v253
	global_load_dwordx4 v[114:117], v253, s[4:5]
	global_load_dwordx4 v[118:121], v253, s[4:5] offset:1024
	v_add_u32_e32 v253, 0x2000, v253
	global_load_dwordx4 v[122:125], v253, s[4:5]
	global_load_dwordx4 v[126:129], v253, s[4:5] offset:1024
	v_add_u32_e32 v253, 0x2000, v253
	global_load_dwordx4 v[130:133], v253, s[4:5]
	global_load_dwordx4 v[134:137], v253, s[4:5] offset:1024
	s_waitcnt vmcnt(34)
	ds_write_b128 v248, v[138:141]
	ds_write_b128 v248, v[142:145] offset:1024
	ds_write_b128 v248, v[146:149] offset:2048
	ds_write_b128 v248, v[150:153] offset:3072
	s_waitcnt vmcnt(34) lgkmcnt(0)
	s_barrier
.Lg_top:
	s_sub_u32 s18, s10, 2
	s_cmp_lt_u32 s18, s9
	s_cbranch_scc0 .Lg_s2skip0
	s_waitcnt vmcnt(21)
	v_cvt_pk_f16_f32 v250, v138, v139
	v_cvt_pk_f16_f32 v251, v140, v141
	ds_write_b64 v241, v[250:251] offset:0
	s_waitcnt vmcnt(20)
	v_cvt_pk_f16_f32 v252, v142, v143
	v_cvt_pk_f16_f32 v253, v144, v145
	ds_write_b64 v241, v[252:253] offset:600
	s_waitcnt vmcnt(19)
	v_cvt_pk_f16_f32 v250, v146, v147
	v_cvt_pk_f16_f32 v251, v148, v149
	ds_write_b64 v241, v[250:251] offset:1248
	s_waitcnt vmcnt(18)
	v_cvt_pk_f16_f32 v252, v150, v151
	v_cvt_pk_f16_f32 v253, v152, v153
	ds_write_b64 v241, v[252:253] offset:1848
	s_waitcnt vmcnt(17)
	v_cvt_pk_f16_f32 v250, v154, v155
	v_cvt_pk_f16_f32 v251, v156, v157
	ds_write_b64 v241, v[250:251] offset:2496
	s_waitcnt vmcnt(16)
	v_cvt_pk_f16_f32 v252, v158, v159
	v_cvt_pk_f16_f32 v253, v160, v161
	ds_write_b64 v241, v[252:253] offset:3096
	s_waitcnt vmcnt(15)
	v_cvt_pk_f16_f32 v250, v162, v163
	v_cvt_pk_f16_f32 v251, v164, v165
	ds_write_b64 v241, v[250:251] offset:3744
	s_waitcnt vmcnt(14)
	v_cvt_pk_f16_f32 v252, v166, v167
	v_cvt_pk_f16_f32 v253, v168, v169
	ds_write_b64 v241, v[252:253] offset:4344
	s_mov_b64 exec, s[34:35]
	s_waitcnt vmcnt(13)
	v_cvt_pk_f16_f32 v250, v170, v171
	v_cvt_pk_f16_f32 v251, v172, v173
	ds_write_b64 v242, v[250:251] offset:0
	s_waitcnt vmcnt(12)
	v_cvt_pk_f16_f32 v252, v174, v175
	v_cvt_pk_f16_f32 v253, v176, v177
	ds_write_b64 v242, v[252:253] offset:600
	s_mov_b64 exec, -1
.Lg_s2skip0:
	v_readlane_b32 s13, v247, s10
	s_add_u32 s14, s12, 0x4b0
	s_add_u32 s15, s12, 0x960
	s_add_u32 s16, s12, 0xe10
	s_nop 1
	s_and_b32 s18, s13, 0xff
	s_cmp_eq_u32 s18, 1
	s_cselect_b32 s42, s12, 0x80000000
	s_and_b32 s18, s13, 0xff00
	s_cmp_eq_u32 s18, 0x100
	s_cselect_b32 s14, s14, 0x80000000
	s_and_b32 s18, s13, 0xff0000
	s_cmp_eq_u32 s18, 0x10000
	s_cselect_b32 s15, s15, 0x80000000
	s_and_b32 s18, s13, 0xff000000
	s_cmp_eq_u32 s18, 0x1000000
	s_cselect_b32 s16, s16, 0x80000000
	v_lshrrev_b32_e64 v253, v240, s13
	v_and_b32_e32 v253, 0xff, v253
	v_cmp_eq_u32_e32 vcc, 1, v253
	s_nop 1
	v_cndmask_b32_e32 v254, v255, v239, vcc
	buffer_load_dwordx4 v[138:141], v238, s[20:23], s42 offen nt
	buffer_load_dwordx4 v[142:145], v238, s[24:27], s42 offen nt
	buffer_load_dwordx4 v[146:149], v238, s[20:23], s14 offen nt
	buffer_load_dwordx4 v[150:153], v238, s[24:27], s14 offen nt
	buffer_load_dwordx4 v[154:157], v238, s[20:23], s15 offen nt
	buffer_load_dwordx4 v[158:161], v238, s[24:27], s15 offen nt
	buffer_load_dwordx4 v[162:165], v238, s[20:23], s16 offen nt
	buffer_load_dwordx4 v[166:169], v238, s[24:27], s16 offen nt
	buffer_load_dwordx4 v[170:173], v254, s[20:23], s12 offen nt
	buffer_load_dwordx4 v[174:177], v254, s[24:27], s12 offen nt
	s_add_u32 s12, s12, 0x12c000
	s_sub_u32 s18, s10, 3
	s_cmp_lt_u32 s18, s9
	s_cbranch_scc0 .Lg_s3skip0
	ds_read_b128 v[226:229], v243 offset:21056
	ds_read_b128 v[230:233], v248
	ds_read_b128 v[234:237], v248 offset:1024
	s_waitcnt lgkmcnt(0)
	v_mfma_f32_16x16x32_f16 v[218:221], v[226:229], v[230:233], 0
	v_mfma_f32_16x16x32_f16 v[222:225], v[226:229], v[234:237], 0
	ds_read_b128 v[226:229], v243 offset:21120
	ds_read_b128 v[230:233], v248 offset:2048
	ds_read_b128 v[234:237], v248 offset:3072
	s_waitcnt lgkmcnt(0)
	v_mfma_f32_16x16x32_f16 v[218:221], v[226:229], v[230:233], v[218:221]
	v_mfma_f32_16x16x32_f16 v[222:225], v[226:229], v[234:237], v[222:225]
	ds_read_b128 v[226:229], v243 offset:19968
	ds_read_b128 v[230:233], v243 offset:20032
	ds_read_b128 v[234:237], v243 offset:20096
	s_waitcnt lgkmcnt(2)
	v_mfma_f32_16x16x32_f16 v[218:221], v[226:229], v[2:5], v[218:221]
	v_mfma_f32_16x16x32_f16 v[222:225], v[226:229], v[6:9], v[222:225]
	ds_read_b128 v[226:229], v243 offset:20160
	s_waitcnt lgkmcnt(2)
	v_mfma_f32_16x16x32_f16 v[218:221], v[230:233], v[10:13], v[218:221]
	v_mfma_f32_16x16x32_f16 v[222:225], v[230:233], v[14:17], v[222:225]
	ds_read_b128 v[230:233], v243 offset:20224
	s_waitcnt lgkmcnt(2)
	v_mfma_f32_16x16x32_f16 v[218:221], v[234:237], v[18:21], v[218:221]
	v_mfma_f32_16x16x32_f16 v[222:225], v[234:237], v[22:25], v[222:225]
	ds_read_b128 v[234:237], v243 offset:20288
	s_waitcnt lgkmcnt(2)
	v_mfma_f32_16x16x32_f16 v[218:221], v[226:229], v[26:29], v[218:221]
	v_mfma_f32_16x16x32_f16 v[222:225], v[226:229], v[30:33], v[222:225]
	ds_read_b128 v[226:229], v243 offset:20352
	s_waitcnt lgkmcnt(2)
	v_mfma_f32_16x16x32_f16 v[218:221], v[230:233], v[34:37], v[218:221]
	v_mfma_f32_16x16x32_f16 v[222:225], v[230:233], v[38:41], v[222:225]
	ds_read_b128 v[230:233], v243 offset:20416
	s_waitcnt lgkmcnt(2)
	v_mfma_f32_16x16x32_f16 v[218:221], v[234:237], v[42:45], v[218:221]
	v_mfma_f32_16x16x32_f16 v[222:225], v[234:237], v[46:49], v[222:225]
	ds_read_b128 v[234:237], v243 offset:20480
	s_waitcnt lgkmcnt(2)
	v_mfma_f32_16x16x32_f16 v[218:221], v[226:229], v[50:53], v[218:221]
	v_mfma_f32_16x16x32_f16 v[222:225], v[226:229], v[54:57], v[222:225]
	ds_read_b128 v[226:229], v243 offset:20544
	s_waitcnt lgkmcnt(2)
	v_mfma_f32_16x16x32_f16 v[218:221], v[230:233], v[58:61], v[218:221]
	v_mfma_f32_16x16x32_f16 v[222:225], v[230:233], v[62:65], v[222:225]
	ds_read_b128 v[230:233], v243 offset:20608
	s_waitcnt lgkmcnt(2)
	v_mfma_f32_16x16x32_f16 v[218:221], v[234:237], v[66:69], v[218:221]
	v_mfma_f32_16x16x32_f16 v[222:225], v[234:237], v[70:73], v[222:225]
	ds_read_b128 v[234:237], v243 offset:20672
	s_waitcnt lgkmcnt(2)
	v_mfma_f32_16x16x32_f16 v[218:221], v[226:229], v[74:77], v[218:221]
	v_mfma_f32_16x16x32_f16 v[222:225], v[226:229], v[78:81], v[222:225]
	ds_read_b128 v[226:229], v243 offset:20736
	s_waitcnt lgkmcnt(2)
	v_mfma_f32_16x16x32_f16 v[218:221], v[230:233], v[82:85], v[218:221]
	v_mfma_f32_16x16x32_f16 v[222:225], v[230:233], v[86:89], v[222:225]
	ds_read_b128 v[230:233], v243 offset:20800
	s_waitcnt lgkmcnt(2)
	v_mfma_f32_16x16x32_f16 v[218:221], v[234:237], v[90:93], v[218:221]
	v_mfma_f32_16x16x32_f16 v[222:225], v[234:237], v[94:97], v[222:225]
	ds_read_b128 v[234:237], v243 offset:20864
	s_waitcnt lgkmcnt(2)
	v_mfma_f32_16x16x32_f16 v[218:221], v[226:229], v[98:101], v[218:221]
	v_mfma_f32_16x16x32_f16 v[222:225], v[226:229], v[102:105], v[222:225]
	ds_read_b128 v[226:229], v243 offset:20928
	s_waitcnt lgkmcnt(2)
	v_mfma_f32_16x16x32_f16 v[218:221], v[230:233], v[106:109], v[218:221]
	v_mfma_f32_16x16x32_f16 v[222:225], v[230:233], v[110:113], v[222:225]
	ds_read_b128 v[230:233], v243 offset:20992
	s_waitcnt lgkmcnt(2)
	v_mfma_f32_16x16x32_f16 v[218:221], v[234:237], v[114:117], v[218:221]
	v_mfma_f32_16x16x32_f16 v[222:225], v[234:237], v[118:121], v[222:225]
	s_waitcnt lgkmcnt(1)
	v_mfma_f32_16x16x32_f16 v[218:221], v[226:229], v[122:125], v[218:221]
	v_mfma_f32_16x16x32_f16 v[222:225], v[226:229], v[126:129], v[222:225]
	s_waitcnt lgkmcnt(0)
	v_mfma_f32_16x16x32_f16 v[218:221], v[230:233], v[130:133], v[218:221]
	v_mfma_f32_16x16x32_f16 v[222:225], v[230:233], v[134:137], v[222:225]
	s_nop 7
	s_nop 3
	v_cvt_f16_f32_e32 v249, v218
	v_cvt_f16_f32_e32 v250, v219
	v_cvt_f16_f32_e32 v251, v220
	v_cvt_f16_f32_e32 v252, v221
	ds_write_b16 v244, v249 offset:4352
	ds_write_b16 v244, v250 offset:4624
	ds_write_b16 v244, v251 offset:4896
	ds_write_b16 v244, v252 offset:5168
	v_cvt_f16_f32_e32 v249, v222
	v_cvt_f16_f32_e32 v250, v223
	v_cvt_f16_f32_e32 v251, v224
	v_cvt_f16_f32_e32 v252, v225
	ds_write_b16 v244, v249 offset:4384
	ds_write_b16 v244, v250 offset:4656
	ds_write_b16 v244, v251 offset:4928
	ds_write_b16 v244, v252 offset:5200
.Lg_s3skip0:
	s_sub_u32 s18, s10, 4
	s_cmp_lt_u32 s18, s9
	s_cselect_b32 s19, s32, 0x80000000
	ds_read_b128 v[226:229], v245 offset:0
	s_add_u32 s32, s32, 0x40000
	s_waitcnt lgkmcnt(0)
	buffer_store_dwordx4 v[226:229], v246, s[28:31], s19 offen nt
	s_barrier
	s_add_u32 s10, s10, 1
	s_cmp_ge_u32 s10, s11
	s_cbranch_scc1 .Lg_end
	s_sub_u32 s18, s10, 2
	s_cmp_lt_u32 s18, s9
	s_cbranch_scc0 .Lg_s2skip1
	s_waitcnt vmcnt(21)
	v_cvt_pk_f16_f32 v250, v178, v179
	v_cvt_pk_f16_f32 v251, v180, v181
	ds_write_b64 v241, v[250:251] offset:19968
	s_waitcnt vmcnt(20)
	v_cvt_pk_f16_f32 v252, v182, v183
	v_cvt_pk_f16_f32 v253, v184, v185
	ds_write_b64 v241, v[252:253] offset:20568
	s_waitcnt vmcnt(19)
	v_cvt_pk_f16_f32 v250, v186, v187
	v_cvt_pk_f16_f32 v251, v188, v189
	ds_write_b64 v241, v[250:251] offset:21216
	s_waitcnt vmcnt(18)
	v_cvt_pk_f16_f32 v252, v190, v191
	v_cvt_pk_f16_f32 v253, v192, v193
	ds_write_b64 v241, v[252:253] offset:21816
	s_waitcnt vmcnt(17)
	v_cvt_pk_f16_f32 v250, v194, v195
	v_cvt_pk_f16_f32 v251, v196, v197
	ds_write_b64 v241, v[250:251] offset:22464
	s_waitcnt vmcnt(16)
	v_cvt_pk_f16_f32 v252, v198, v199
	v_cvt_pk_f16_f32 v253, v200, v201
	ds_write_b64 v241, v[252:253] offset:23064
	s_waitcnt vmcnt(15)
	v_cvt_pk_f16_f32 v250, v202, v203
	v_cvt_pk_f16_f32 v251, v204, v205
	ds_write_b64 v241, v[250:251] offset:23712
	s_waitcnt vmcnt(14)
	v_cvt_pk_f16_f32 v252, v206, v207
	v_cvt_pk_f16_f32 v253, v208, v209
	ds_write_b64 v241, v[252:253] offset:24312
	s_mov_b64 exec, s[34:35]
	s_waitcnt vmcnt(13)
	v_cvt_pk_f16_f32 v250, v210, v211
	v_cvt_pk_f16_f32 v251, v212, v213
	ds_write_b64 v242, v[250:251] offset:19968
	s_waitcnt vmcnt(12)
	v_cvt_pk_f16_f32 v252, v214, v215
	v_cvt_pk_f16_f32 v253, v216, v217
	ds_write_b64 v242, v[252:253] offset:20568
	s_mov_b64 exec, -1
.Lg_s2skip1:
	v_readlane_b32 s13, v247, s10
	s_add_u32 s14, s12, 0x4b0
	s_add_u32 s15, s12, 0x960
	s_add_u32 s16, s12, 0xe10
	s_nop 1
	s_and_b32 s18, s13, 0xff
	s_cmp_eq_u32 s18, 1
	s_cselect_b32 s42, s12, 0x80000000
	s_and_b32 s18, s13, 0xff00
	s_cmp_eq_u32 s18, 0x100
	s_cselect_b32 s14, s14, 0x80000000
	s_and_b32 s18, s13, 0xff0000
	s_cmp_eq_u32 s18, 0x10000
	s_cselect_b32 s15, s15, 0x80000000
	s_and_b32 s18, s13, 0xff000000
	s_cmp_eq_u32 s18, 0x1000000
	s_cselect_b32 s16, s16, 0x80000000
	v_lshrrev_b32_e64 v253, v240, s13
	v_and_b32_e32 v253, 0xff, v253
	v_cmp_eq_u32_e32 vcc, 1, v253
	s_nop 1
	v_cndmask_b32_e32 v254, v255, v239, vcc
	buffer_load_dwordx4 v[178:181], v238, s[20:23], s42 offen nt
	buffer_load_dwordx4 v[182:185], v238, s[24:27], s42 offen nt
	buffer_load_dwordx4 v[186:189], v238, s[20:23], s14 offen nt
	buffer_load_dwordx4 v[190:193], v238, s[24:27], s14 offen nt
	buffer_load_dwordx4 v[194:197], v238, s[20:23], s15 offen nt
	buffer_load_dwordx4 v[198:201], v238, s[24:27], s15 offen nt
	buffer_load_dwordx4 v[202:205], v238, s[20:23], s16 offen nt
	buffer_load_dwordx4 v[206:209], v238, s[24:27], s16 offen nt
	buffer_load_dwordx4 v[210:213], v254, s[20:23], s12 offen nt
	buffer_load_dwordx4 v[214:217], v254, s[24:27], s12 offen nt
	s_add_u32 s12, s12, 0x12c000
	s_sub_u32 s18, s10, 3
	s_cmp_lt_u32 s18, s9
	s_cbranch_scc0 .Lg_s3skip1
	ds_read_b128 v[226:229], v243 offset:1088
	ds_read_b128 v[230:233], v248
	ds_read_b128 v[234:237], v248 offset:1024
	s_waitcnt lgkmcnt(0)
	v_mfma_f32_16x16x32_f16 v[218:221], v[226:229], v[230:233], 0
	v_mfma_f32_16x16x32_f16 v[222:225], v[226:229], v[234:237], 0
	ds_read_b128 v[226:229], v243 offset:1152
	ds_read_b128 v[230:233], v248 offset:2048
	ds_read_b128 v[234:237], v248 offset:3072
	s_waitcnt lgkmcnt(0)
	v_mfma_f32_16x16x32_f16 v[218:221], v[226:229], v[230:233], v[218:221]
	v_mfma_f32_16x16x32_f16 v[222:225], v[226:229], v[234:237], v[222:225]
	ds_read_b128 v[226:229], v243 offset:0
	ds_read_b128 v[230:233], v243 offset:64
	ds_read_b128 v[234:237], v243 offset:128
	s_waitcnt lgkmcnt(2)
	v_mfma_f32_16x16x32_f16 v[218:221], v[226:229], v[2:5], v[218:221]
	v_mfma_f32_16x16x32_f16 v[222:225], v[226:229], v[6:9], v[222:225]
	ds_read_b128 v[226:229], v243 offset:192
	s_waitcnt lgkmcnt(2)
	v_mfma_f32_16x16x32_f16 v[218:221], v[230:233], v[10:13], v[218:221]
	v_mfma_f32_16x16x32_f16 v[222:225], v[230:233], v[14:17], v[222:225]
	ds_read_b128 v[230:233], v243 offset:256
	s_waitcnt lgkmcnt(2)
	v_mfma_f32_16x16x32_f16 v[218:221], v[234:237], v[18:21], v[218:221]
	v_mfma_f32_16x16x32_f16 v[222:225], v[234:237], v[22:25], v[222:225]
	ds_read_b128 v[234:237], v243 offset:320
	s_waitcnt lgkmcnt(2)
	v_mfma_f32_16x16x32_f16 v[218:221], v[226:229], v[26:29], v[218:221]
	v_mfma_f32_16x16x32_f16 v[222:225], v[226:229], v[30:33], v[222:225]
	ds_read_b128 v[226:229], v243 offset:384
	s_waitcnt lgkmcnt(2)
	v_mfma_f32_16x16x32_f16 v[218:221], v[230:233], v[34:37], v[218:221]
	v_mfma_f32_16x16x32_f16 v[222:225], v[230:233], v[38:41], v[222:225]
	ds_read_b128 v[230:233], v243 offset:448
	s_waitcnt lgkmcnt(2)
	v_mfma_f32_16x16x32_f16 v[218:221], v[234:237], v[42:45], v[218:221]
	v_mfma_f32_16x16x32_f16 v[222:225], v[234:237], v[46:49], v[222:225]
	ds_read_b128 v[234:237], v243 offset:512
	s_waitcnt lgkmcnt(2)
	v_mfma_f32_16x16x32_f16 v[218:221], v[226:229], v[50:53], v[218:221]
	v_mfma_f32_16x16x32_f16 v[222:225], v[226:229], v[54:57], v[222:225]
	ds_read_b128 v[226:229], v243 offset:576
	s_waitcnt lgkmcnt(2)
	v_mfma_f32_16x16x32_f16 v[218:221], v[230:233], v[58:61], v[218:221]
	v_mfma_f32_16x16x32_f16 v[222:225], v[230:233], v[62:65], v[222:225]
	ds_read_b128 v[230:233], v243 offset:640
	s_waitcnt lgkmcnt(2)
	v_mfma_f32_16x16x32_f16 v[218:221], v[234:237], v[66:69], v[218:221]
	v_mfma_f32_16x16x32_f16 v[222:225], v[234:237], v[70:73], v[222:225]
	ds_read_b128 v[234:237], v243 offset:704
	s_waitcnt lgkmcnt(2)
	v_mfma_f32_16x16x32_f16 v[218:221], v[226:229], v[74:77], v[218:221]
	v_mfma_f32_16x16x32_f16 v[222:225], v[226:229], v[78:81], v[222:225]
	ds_read_b128 v[226:229], v243 offset:768
	s_waitcnt lgkmcnt(2)
	v_mfma_f32_16x16x32_f16 v[218:221], v[230:233], v[82:85], v[218:221]
	v_mfma_f32_16x16x32_f16 v[222:225], v[230:233], v[86:89], v[222:225]
	ds_read_b128 v[230:233], v243 offset:832
	s_waitcnt lgkmcnt(2)
	v_mfma_f32_16x16x32_f16 v[218:221], v[234:237], v[90:93], v[218:221]
	v_mfma_f32_16x16x32_f16 v[222:225], v[234:237], v[94:97], v[222:225]
	ds_read_b128 v[234:237], v243 offset:896
	s_waitcnt lgkmcnt(2)
	v_mfma_f32_16x16x32_f16 v[218:221], v[226:229], v[98:101], v[218:221]
	v_mfma_f32_16x16x32_f16 v[222:225], v[226:229], v[102:105], v[222:225]
	ds_read_b128 v[226:229], v243 offset:960
	s_waitcnt lgkmcnt(2)
	v_mfma_f32_16x16x32_f16 v[218:221], v[230:233], v[106:109], v[218:221]
	v_mfma_f32_16x16x32_f16 v[222:225], v[230:233], v[110:113], v[222:225]
	ds_read_b128 v[230:233], v243 offset:1024
	s_waitcnt lgkmcnt(2)
	v_mfma_f32_16x16x32_f16 v[218:221], v[234:237], v[114:117], v[218:221]
	v_mfma_f32_16x16x32_f16 v[222:225], v[234:237], v[118:121], v[222:225]
	s_waitcnt lgkmcnt(1)
	v_mfma_f32_16x16x32_f16 v[218:221], v[226:229], v[122:125], v[218:221]
	v_mfma_f32_16x16x32_f16 v[222:225], v[226:229], v[126:129], v[222:225]
	s_waitcnt lgkmcnt(0)
	v_mfma_f32_16x16x32_f16 v[218:221], v[230:233], v[130:133], v[218:221]
	v_mfma_f32_16x16x32_f16 v[222:225], v[230:233], v[134:137], v[222:225]
	s_nop 7
	s_nop 3
	v_cvt_f16_f32_e32 v249, v218
	v_cvt_f16_f32_e32 v250, v219
	v_cvt_f16_f32_e32 v251, v220
	v_cvt_f16_f32_e32 v252, v221
	ds_write_b16 v244, v249 offset:0
	ds_write_b16 v244, v250 offset:272
	ds_write_b16 v244, v251 offset:544
	ds_write_b16 v244, v252 offset:816
	v_cvt_f16_f32_e32 v249, v222
	v_cvt_f16_f32_e32 v250, v223
	v_cvt_f16_f32_e32 v251, v224
	v_cvt_f16_f32_e32 v252, v225
	ds_write_b16 v244, v249 offset:32
	ds_write_b16 v244, v250 offset:304
	ds_write_b16 v244, v251 offset:576
	ds_write_b16 v244, v252 offset:848
.Lg_s3skip1:
	s_sub_u32 s18, s10, 4
	s_cmp_lt_u32 s18, s9
	s_cselect_b32 s19, s32, 0x80000000
	ds_read_b128 v[226:229], v245 offset:4352
	s_add_u32 s32, s32, 0x40000
	s_waitcnt lgkmcnt(0)
	buffer_store_dwordx4 v[226:229], v246, s[28:31], s19 offen nt
	s_barrier
	s_add_u32 s10, s10, 1
	s_cmp_lt_u32 s10, s11
	s_cbranch_scc1 .Lg_top

	.amdhsa_kernel _Z6k_gemmPKfS0_PK15HIP_vector_typeIjLj4EEPDF16_PKh
		.amdhsa_group_segment_fixed_size 16384
		.amdhsa_private_segment_fixed_size 0
		.amdhsa_kernarg_size 40
		.amdhsa_user_sgpr_count 2
		.amdhsa_user_sgpr_dispatch_ptr 0
		.amdhsa_user_sgpr_queue_ptr 0
		.amdhsa_user_sgpr_kernarg_segment_ptr 1
		.amdhsa_user_sgpr_dispatch_id 0
		.amdhsa_user_sgpr_kernarg_preload_length 0
		.amdhsa_user_sgpr_kernarg_preload_offset 0
		.amdhsa_user_sgpr_private_segment_size 0
		.amdhsa_uses_dynamic_stack 0
		.amdhsa_enable_private_segment 0
		.amdhsa_system_sgpr_workgroup_id_x 1
		.amdhsa_system_sgpr_workgroup_id_y 0
		.amdhsa_system_sgpr_workgroup_id_z 0
		.amdhsa_system_sgpr_workgroup_info 0
		.amdhsa_system_vgpr_workitem_id 0
		.amdhsa_next_free_vgpr 256
		.amdhsa_next_free_sgpr 44
		.amdhsa_accum_offset 256
		.amdhsa_reserve_vcc 1
		.amdhsa_float_round_mode_32 0
		.amdhsa_float_round_mode_16_64 0
		.amdhsa_float_denorm_mode_32 3
		.amdhsa_float_denorm_mode_16_64 3
		.amdhsa_dx10_clamp 1
		.amdhsa_ieee_mode 1
		.amdhsa_fp16_overflow 0
		.amdhsa_tg_split 0
		.amdhsa_exception_fp_ieee_invalid_op 0
		.amdhsa_exception_fp_denorm_src 0
		.amdhsa_exception_fp_ieee_div_zero 0
		.amdhsa_exception_fp_ieee_overflow 0
		.amdhsa_exception_fp_ieee_underflow 0
		.amdhsa_exception_fp_ieee_inexact 0
		.amdhsa_exception_int_div_zero 0
	.end_amdhsa_kernel

amdhsa.kernels:
  - .agpr_count:     0
    .args:
      - .actual_access:  read_only
        .address_space:  global
        .offset:         0
        .size:           8
        .value_kind:     global_buffer
      - .actual_access:  read_only
        .address_space:  global
        .offset:         8
        .size:           8
        .value_kind:     global_buffer
      - .actual_access:  write_only
        .address_space:  global
        .offset:         16
        .size:           8
        .value_kind:     global_buffer
      - .actual_access:  write_only
        .address_space:  global
        .offset:         24
        .size:           8
        .value_kind:     global_buffer
      - .actual_access:  write_only
        .address_space:  global
        .offset:         32
        .size:           8
        .value_kind:     global_buffer
      - .actual_access:  write_only
        .address_space:  global
        .offset:         40
        .size:           8
        .value_kind:     global_buffer
    .group_segment_fixed_size: 32
    .kernarg_segment_align: 8
    .kernarg_segment_size: 48
    .language:       OpenCL C
    .language_version:
      - 2
      - 0
    .max_flat_workgroup_size: 512
    .name:           _Z6k_prepPKiPKfPiS3_P15HIP_vector_typeIjLj4EEPh
    .private_segment_fixed_size: 0
    .sgpr_count:     16
    .sgpr_spill_count: 0
    .symbol:         _Z6k_prepPKiPKfPiS3_P15HIP_vector_typeIjLj4EEPh.kd
    .uniform_work_group_size: 1
    .uses_dynamic_stack: false
    .vgpr_count:     36
    .vgpr_spill_count: 0
    .wavefront_size: 64
  - .agpr_count:     0
    .args:
      - .actual_access:  read_only
        .address_space:  global
        .offset:         0
        .size:           8
        .value_kind:     global_buffer
      - .actual_access:  read_only
        .address_space:  global
        .offset:         8
        .size:           8
        .value_kind:     global_buffer
      - .actual_access:  read_only
        .address_space:  global
        .offset:         16
        .size:           8
        .value_kind:     global_buffer
      - .actual_access:  write_only
        .address_space:  global
        .offset:         24
        .size:           8
        .value_kind:     global_buffer
      - .actual_access:  read_only
        .address_space:  global
        .offset:         32
        .size:           8
        .value_kind:     global_buffer
    .group_segment_fixed_size: 16384
    .kernarg_segment_align: 8
    .kernarg_segment_size: 40
    .language:       OpenCL C
    .language_version:
      - 2
      - 0
    .max_flat_workgroup_size: 256
    .name:           _Z6k_gemmPKfS0_PK15HIP_vector_typeIjLj4EEPDF16_PKh
    .private_segment_fixed_size: 0
    .sgpr_count:     50
    .sgpr_spill_count: 0
    .symbol:         _Z6k_gemmPKfS0_PK15HIP_vector_typeIjLj4EEPDF16_PKh.kd
    .uniform_work_group_size: 1
    .uses_dynamic_stack: false
    .vgpr_count:     256
    .vgpr_spill_count: 0
    .wavefront_size: 64
  - .agpr_count:     0
    .args:
      - .actual_access:  read_only
        .address_space:  global
        .offset:         0
        .size:           8
        .value_kind:     global_buffer
      - .actual_access:  read_only
        .address_space:  global
        .offset:         8
        .size:           8
        .value_kind:     global_buffer
      - .actual_access:  read_only
        .address_space:  global
        .offset:         16
        .size:           8
        .value_kind:     global_buffer
      - .actual_access:  read_only
        .address_space:  global
        .offset:         24
        .size:           8
        .value_kind:     global_buffer
      - .actual_access:  read_only
        .address_space:  global
        .offset:         32
        .size:           8
        .value_kind:     global_buffer
      - .actual_access:  read_only
        .address_space:  global
        .offset:         40
        .size:           8
        .value_kind:     global_buffer
      - .actual_access:  write_only
        .address_space:  global
        .offset:         48
        .size:           8
        .value_kind:     global_buffer
    .group_segment_fixed_size: 4096
    .kernarg_segment_align: 8
    .kernarg_segment_size: 56
    .language:       OpenCL C
    .language_version:
      - 2
      - 0
    .max_flat_workgroup_size: 1024
    .name:           _Z6k_poolPKDF16_PKiS2_PKfS4_S4_Pf
    .private_segment_fixed_size: 0
    .sgpr_count:     30
    .sgpr_spill_count: 0
    .symbol:         _Z6k_poolPKDF16_PKiS2_PKfS4_S4_Pf.kd
    .uniform_work_group_size: 1
    .uses_dynamic_stack: false
    .vgpr_count:     64
    .vgpr_spill_count: 0
    .wavefront_size: 64
